# attention loops: lgkmcnt wait ladders collapsed, no-op s_add removed
# speedup vs baseline: 1.0015x; 1.0015x over previous
.LBB0_632:
	s_bitcmp1_b32 s12, 0
	s_cselect_b32 s14, 0, 0x5400
	s_cselect_b32 s13, 0x5400, 0
	v_add3_u32 v234, s14, v220, v223
	global_load_dwordx4 v[158:161], v[194:195], off offset:-256
	global_load_dwordx4 v[162:165], v[194:195], off
	ds_read_b128 v[206:209], v234
	ds_read_b128 v[210:213], v234 offset:32
	ds_read_b128 v[226:229], v234 offset:64
	ds_read_b128 v[230:233], v234 offset:96
	s_waitcnt lgkmcnt(0)
	v_add_u32_e32 v225, s14, v221
	v_mfma_f32_32x32x16_bf16 v[96:111], v[206:209], v[134:137], 0.5
	v_add3_u32 v225, v225, v222, v224
	s_add_i32 s12, s12, 1
	s_add_i32 s14, s4, s12
	v_lshl_add_u64 v[194:195], v[194:195], 0, s[84:85]
	s_cmp_eq_u32 s14, 2
	v_mfma_f32_32x32x16_bf16 v[80:95], v[206:209], v[118:121], 0.5
	v_mfma_f32_32x32x16_bf16 v[96:111], v[210:213], v[138:141], v[96:111]
	v_mfma_f32_32x32x16_bf16 v[80:95], v[210:213], v[122:125], v[80:95]
	v_mfma_f32_32x32x16_bf16 v[96:111], v[226:229], v[142:145], v[96:111]
	v_mfma_f32_32x32x16_bf16 v[80:95], v[226:229], v[126:129], v[80:95]
	v_mfma_f32_32x32x16_bf16 v[96:111], v[230:233], v[146:149], v[96:111]
	v_mfma_f32_32x32x16_bf16 v[80:95], v[230:233], v[130:133], v[80:95]
	ds_read_b64_tr_b16 v[206:207], v225 offset:9216
	ds_read_b64_tr_b16 v[208:209], v225 offset:10752
	ds_read_b64_tr_b16 v[210:211], v225 offset:12288
	ds_read_b64_tr_b16 v[212:213], v225 offset:13824
	ds_read_b64_tr_b16 v[226:227], v225 offset:9280
	ds_read_b64_tr_b16 v[228:229], v225 offset:10816
	ds_read_b64_tr_b16 v[230:231], v225 offset:12352
	ds_read_b64_tr_b16 v[232:233], v225 offset:13888
	s_nop 2
	v_cvt_pknorm_i16_f32 v96, v96, v97
	v_cvt_pknorm_i16_f32 v97, v98, v99
	v_cvt_pknorm_i16_f32 v98, v100, v101
	v_cvt_pknorm_i16_f32 v99, v102, v103
	v_cvt_pknorm_i16_f32 v104, v104, v105
	v_cvt_pknorm_i16_f32 v105, v106, v107
	v_cvt_pknorm_i16_f32 v80, v80, v81
	v_cvt_pknorm_i16_f32 v81, v82, v83
	v_cvt_pknorm_i16_f32 v82, v84, v85
	v_cvt_pknorm_i16_f32 v83, v86, v87
	s_waitcnt lgkmcnt(6)
	v_mfma_f32_32x32x16_bf16 v[48:63], v[206:209], v[96:99], v[48:63]
	v_cvt_pknorm_i16_f32 v106, v108, v109
	v_cvt_pknorm_i16_f32 v107, v110, v111
	v_cvt_pknorm_i16_f32 v88, v88, v89
	v_cvt_pknorm_i16_f32 v89, v90, v91
	v_cvt_pknorm_i16_f32 v90, v92, v93
	v_cvt_pknorm_i16_f32 v91, v94, v95
	s_waitcnt lgkmcnt(2)
	v_mfma_f32_32x32x16_bf16 v[32:47], v[226:229], v[96:99], v[32:47]
	v_mfma_f32_32x32x16_bf16 v[16:31], v[206:209], v[80:83], v[16:31]
	v_mfma_f32_32x32x16_bf16 v[0:15], v[226:229], v[80:83], v[0:15]
	v_mfma_f32_16x16x32_bf16 v[100:103], v[114:117], v[96:99], v[150:153]
	v_mfma_f32_16x16x32_bf16 v[84:87], v[114:117], v[80:83], v[154:157]
	v_mfma_f32_32x32x16_bf16 v[48:63], v[210:213], v[104:107], v[48:63]
	s_waitcnt lgkmcnt(0)
	v_mfma_f32_32x32x16_bf16 v[32:47], v[230:233], v[104:107], v[32:47]
	v_mfma_f32_32x32x16_bf16 v[16:31], v[210:213], v[88:91], v[16:31]
	v_mfma_f32_32x32x16_bf16 v[0:15], v[230:233], v[88:91], v[0:15]
	ds_read_b128 v[206:209], v234 offset:4608
	ds_read_b128 v[210:213], v234 offset:4640
	ds_read_b128 v[226:229], v234 offset:4672
	ds_read_b128 v[230:233], v234 offset:4704
	s_waitcnt lgkmcnt(0)
	v_mfma_f32_16x16x32_bf16 v[150:153], v[114:117], v[104:107], v[100:103]
	v_mfma_f32_16x16x32_bf16 v[154:157], v[114:117], v[88:91], v[84:87]
	v_mfma_f32_32x32x16_bf16 v[96:111], v[206:209], v[134:137], 0.5
	v_mfma_f32_32x32x16_bf16 v[80:95], v[206:209], v[118:121], 0.5
	ds_read_b64_tr_b16 v[64:65], v225 offset:15360
	ds_read_b64_tr_b16 v[66:67], v225 offset:16896
	ds_read_b64_tr_b16 v[68:69], v225 offset:18432
	ds_read_b64_tr_b16 v[70:71], v225 offset:19968
	ds_read_b64_tr_b16 v[72:73], v225 offset:15424
	ds_read_b64_tr_b16 v[74:75], v225 offset:16960
	ds_read_b64_tr_b16 v[76:77], v225 offset:18496
	ds_read_b64_tr_b16 v[78:79], v225 offset:20032
	v_mfma_f32_32x32x16_bf16 v[96:111], v[210:213], v[138:141], v[96:111]
	v_mfma_f32_32x32x16_bf16 v[80:95], v[210:213], v[122:125], v[80:95]
	v_mfma_f32_32x32x16_bf16 v[96:111], v[226:229], v[142:145], v[96:111]
	v_mfma_f32_32x32x16_bf16 v[80:95], v[226:229], v[126:129], v[80:95]
	v_mfma_f32_32x32x16_bf16 v[96:111], v[230:233], v[146:149], v[96:111]
	v_mfma_f32_32x32x16_bf16 v[80:95], v[230:233], v[130:133], v[80:95]
	s_nop 10
	v_cvt_pknorm_i16_f32 v96, v96, v97
	v_cvt_pknorm_i16_f32 v97, v98, v99
	v_cvt_pknorm_i16_f32 v98, v100, v101
	v_cvt_pknorm_i16_f32 v99, v102, v103
	v_cvt_pknorm_i16_f32 v104, v104, v105
	v_cvt_pknorm_i16_f32 v105, v106, v107
	v_cvt_pknorm_i16_f32 v106, v108, v109
	v_cvt_pknorm_i16_f32 v80, v80, v81
	v_cvt_pknorm_i16_f32 v81, v82, v83
	v_cvt_pknorm_i16_f32 v82, v84, v85
	v_cvt_pknorm_i16_f32 v83, v86, v87
	s_waitcnt lgkmcnt(6)
	v_mfma_f32_32x32x16_bf16 v[48:63], v[64:67], v[96:99], v[48:63]
	v_cvt_pknorm_i16_f32 v107, v110, v111
	v_cvt_pknorm_i16_f32 v88, v88, v89
	v_cvt_pknorm_i16_f32 v89, v90, v91
	v_cvt_pknorm_i16_f32 v90, v92, v93
	v_cvt_pknorm_i16_f32 v91, v94, v95
	s_waitcnt lgkmcnt(2)
	v_mfma_f32_32x32x16_bf16 v[32:47], v[72:75], v[96:99], v[32:47]
	v_mfma_f32_32x32x16_bf16 v[16:31], v[64:67], v[80:83], v[16:31]
	v_add3_u32 v64, s13, v217, v218
	v_add3_u32 v65, s13, v219, v218
	s_waitcnt vmcnt(1)
	ds_write_b128 v64, v[158:161]
	s_waitcnt vmcnt(0)
	ds_write_b128 v65, v[162:165] offset:9216
	s_waitcnt lgkmcnt(0)
	s_barrier
	v_mfma_f32_32x32x16_bf16 v[0:15], v[72:75], v[80:83], v[0:15]
	v_mfma_f32_16x16x32_bf16 v[100:103], v[114:117], v[96:99], v[150:153]
	v_mfma_f32_32x32x16_bf16 v[48:63], v[68:71], v[104:107], v[48:63]
	v_mfma_f32_32x32x16_bf16 v[32:47], v[76:79], v[104:107], v[32:47]
	v_mfma_f32_16x16x32_bf16 v[84:87], v[114:117], v[80:83], v[154:157]
	v_mfma_f32_32x32x16_bf16 v[16:31], v[68:71], v[88:91], v[16:31]
	v_mfma_f32_32x32x16_bf16 v[0:15], v[76:79], v[88:91], v[0:15]
	v_mfma_f32_16x16x32_bf16 v[150:153], v[114:117], v[104:107], v[100:103]
	v_mfma_f32_16x16x32_bf16 v[154:157], v[114:117], v[88:91], v[84:87]
	s_cbranch_scc0 .LBB0_632
	v_add3_u32 v194, s13, v220, v223
	v_mov_b64_e32 v[64:65], s[68:69]
	ds_read_b128 v[158:161], v194
	v_mov_b64_e32 v[66:67], s[70:71]
	v_mov_b64_e32 v[68:69], s[72:73]
	v_mov_b64_e32 v[70:71], s[74:75]
	v_mov_b64_e32 v[72:73], s[76:77]
	v_mov_b64_e32 v[74:75], s[78:79]
	v_mov_b64_e32 v[76:77], s[80:81]
	v_mov_b64_e32 v[78:79], s[82:83]
	ds_read_b128 v[162:165], v194 offset:32
	ds_read_b128 v[206:209], v194 offset:64
	ds_read_b128 v[210:213], v194 offset:96
	s_waitcnt lgkmcnt(3)
	s_waitcnt lgkmcnt(2)
	v_mfma_f32_32x32x16_bf16 v[96:111], v[158:161], v[134:137], v[64:79]
	s_waitcnt lgkmcnt(1)
	s_waitcnt lgkmcnt(0)
	v_mfma_f32_32x32x16_bf16 v[80:95], v[158:161], v[118:121], v[64:79]
	v_add_u32_e32 v158, s13, v221
	v_add3_u32 v195, v158, v222, v224
	ds_read_b64_tr_b16 v[158:159], v195 offset:9216
	ds_read_b64_tr_b16 v[160:161], v195 offset:10752
	v_mfma_f32_32x32x16_bf16 v[96:111], v[162:165], v[138:141], v[96:111]
	v_mfma_f32_32x32x16_bf16 v[80:95], v[162:165], v[122:125], v[80:95]
	v_mfma_f32_32x32x16_bf16 v[96:111], v[206:209], v[142:145], v[96:111]
	v_mfma_f32_32x32x16_bf16 v[80:95], v[206:209], v[126:129], v[80:95]
	v_mfma_f32_32x32x16_bf16 v[96:111], v[210:213], v[146:149], v[96:111]
	v_mfma_f32_32x32x16_bf16 v[80:95], v[210:213], v[130:133], v[80:95]
	s_nop 10
	v_cvt_pknorm_i16_f32 v96, v96, v97
	v_cvt_pknorm_i16_f32 v97, v98, v99
	v_cvt_pknorm_i16_f32 v98, v100, v101
	v_cvt_pknorm_i16_f32 v99, v102, v103
	ds_read_b64_tr_b16 v[102:103], v195 offset:10816
	ds_read_b64_tr_b16 v[100:101], v195 offset:9280
	ds_read_b64_tr_b16 v[162:163], v195 offset:12288
	ds_read_b64_tr_b16 v[164:165], v195 offset:13824
	v_cvt_pknorm_i16_f32 v104, v104, v105
	v_cvt_pknorm_i16_f32 v206, v80, v81
	v_cvt_pknorm_i16_f32 v207, v82, v83
	v_cvt_pknorm_i16_f32 v208, v84, v85
	v_cvt_pknorm_i16_f32 v209, v86, v87
	s_waitcnt lgkmcnt(4)
	v_mfma_f32_32x32x16_bf16 v[48:63], v[158:161], v[96:99], v[48:63]
	v_cvt_pknorm_i16_f32 v105, v106, v107
	v_cvt_pknorm_i16_f32 v106, v108, v109
	v_cvt_pknorm_i16_f32 v107, v110, v111
	ds_read_b64_tr_b16 v[110:111], v195 offset:13888
	ds_read_b64_tr_b16 v[108:109], v195 offset:12352
	s_waitcnt lgkmcnt(4)
	v_mfma_f32_32x32x16_bf16 v[32:47], v[100:103], v[96:99], v[32:47]
	v_mfma_f32_32x32x16_bf16 v[16:31], v[158:161], v[206:209], v[16:31]
	v_cvt_pknorm_i16_f32 v158, v88, v89
	v_cvt_pknorm_i16_f32 v159, v90, v91
	v_cvt_pknorm_i16_f32 v160, v92, v93
	v_cvt_pknorm_i16_f32 v161, v94, v95
	v_mfma_f32_32x32x16_bf16 v[0:15], v[100:103], v[206:209], v[0:15]
	s_waitcnt lgkmcnt(2)
	v_mfma_f32_32x32x16_bf16 v[48:63], v[162:165], v[104:107], v[48:63]
	s_waitcnt lgkmcnt(0)
	v_mfma_f32_32x32x16_bf16 v[32:47], v[108:111], v[104:107], v[32:47]
	v_mfma_f32_32x32x16_bf16 v[16:31], v[162:165], v[158:161], v[16:31]
	v_mfma_f32_32x32x16_bf16 v[0:15], v[108:111], v[158:161], v[0:15]
	ds_read_b128 v[100:103], v194 offset:4608
	ds_read_b128 v[108:111], v194 offset:4640
	ds_read_b128 v[162:165], v194 offset:4672
	ds_read_b128 v[210:213], v194 offset:4704
	s_waitcnt lgkmcnt(3)
	s_waitcnt lgkmcnt(2)
	s_waitcnt lgkmcnt(1)
	s_waitcnt lgkmcnt(0)
	v_mfma_f32_32x32x16_bf16 v[80:95], v[100:103], v[134:137], v[64:79]
	v_mfma_f32_32x32x16_bf16 v[64:79], v[100:103], v[118:121], v[64:79]
	ds_read_b64_tr_b16 v[100:101], v195 offset:15360
	ds_read_b64_tr_b16 v[102:103], v195 offset:16896
	v_mfma_f32_32x32x16_bf16 v[80:95], v[108:111], v[138:141], v[80:95]
	v_mfma_f32_32x32x16_bf16 v[64:79], v[108:111], v[122:125], v[64:79]
	v_mfma_f32_32x32x16_bf16 v[80:95], v[162:165], v[142:145], v[80:95]
	v_mfma_f32_32x32x16_bf16 v[64:79], v[162:165], v[126:129], v[64:79]
	v_mfma_f32_32x32x16_bf16 v[80:95], v[210:213], v[146:149], v[80:95]
	v_mfma_f32_32x32x16_bf16 v[64:79], v[210:213], v[130:133], v[64:79]
	s_nop 10
	v_cvt_pknorm_i16_f32 v80, v80, v81
	v_cvt_pknorm_i16_f32 v81, v82, v83
	v_cvt_pknorm_i16_f32 v82, v84, v85
	v_cvt_pknorm_i16_f32 v83, v86, v87
	ds_read_b64_tr_b16 v[86:87], v195 offset:16960
	ds_read_b64_tr_b16 v[84:85], v195 offset:15424
	ds_read_b64_tr_b16 v[108:109], v195 offset:18432
	ds_read_b64_tr_b16 v[110:111], v195 offset:19968
	v_cvt_pknorm_i16_f32 v88, v88, v89
	v_cvt_pknorm_i16_f32 v64, v64, v65
	v_cvt_pknorm_i16_f32 v65, v66, v67
	v_cvt_pknorm_i16_f32 v66, v68, v69
	v_cvt_pknorm_i16_f32 v67, v70, v71
	v_cvt_pknorm_i16_f32 v89, v90, v91
	v_cvt_pknorm_i16_f32 v90, v92, v93
	s_waitcnt lgkmcnt(2)
	v_mfma_f32_32x32x16_bf16 v[0:15], v[84:87], v[64:67], v[0:15]
	v_cvt_pknorm_i16_f32 v91, v94, v95
	ds_read_b64_tr_b16 v[94:95], v195 offset:20032
	ds_read_b64_tr_b16 v[92:93], v195 offset:18496
	v_cvt_pknorm_i16_f32 v68, v72, v73
	v_cvt_pknorm_i16_f32 v69, v74, v75
	v_cvt_pknorm_i16_f32 v70, v76, v77
	v_cvt_pknorm_i16_f32 v71, v78, v79
	s_waitcnt lgkmcnt(0)
	v_mfma_f32_16x16x32_bf16 v[72:75], v[114:117], v[96:99], v[150:153]
	s_barrier
	v_mfma_f32_16x16x32_bf16 v[76:79], v[114:117], v[206:209], v[154:157]
	v_mfma_f32_32x32x16_bf16 v[48:63], v[100:103], v[80:83], v[48:63]
	v_mfma_f32_32x32x16_bf16 v[32:47], v[84:87], v[80:83], v[32:47]
	v_mfma_f32_32x32x16_bf16 v[16:31], v[100:103], v[64:67], v[16:31]
	v_mfma_f32_16x16x32_bf16 v[72:75], v[114:117], v[104:107], v[72:75]
	v_mfma_f32_16x16x32_bf16 v[76:79], v[114:117], v[158:161], v[76:79]
	v_mfma_f32_32x32x16_bf16 v[0:15], v[92:95], v[68:71], v[0:15]
	v_mfma_f32_16x16x32_bf16 v[72:75], v[114:117], v[80:83], v[72:75]
	v_mfma_f32_16x16x32_bf16 v[64:67], v[114:117], v[64:67], v[76:79]
	v_mfma_f32_32x32x16_bf16 v[48:63], v[108:111], v[88:91], v[48:63]
	v_mfma_f32_32x32x16_bf16 v[32:47], v[92:95], v[88:91], v[32:47]
	v_mfma_f32_32x32x16_bf16 v[16:31], v[108:111], v[68:71], v[16:31]
	v_mfma_f32_16x16x32_bf16 v[72:75], v[114:117], v[88:91], v[72:75]
	v_mfma_f32_16x16x32_bf16 v[64:67], v[114:117], v[68:71], v[64:67]
	s_setprio 0
	s_nop 6
	ds_bpermute_b32 v66, v181, v72
	ds_bpermute_b32 v67, v181, v73
	ds_bpermute_b32 v64, v181, v64
	ds_bpermute_b32 v65, v181, v65
	v_lshl_add_u64 v[150:151], v[192:193], 0, s[56:57]
	s_mov_b64 s[46:47], 0
	s_waitcnt lgkmcnt(2)
	v_cndmask_b32_e64 v66, v67, v66, s[40:41]
	v_div_scale_f32 v67, s[12:13], v66, v66, 1.0
	v_rcp_f32_e32 v68, v67
	s_waitcnt lgkmcnt(0)
	v_cndmask_b32_e64 v64, v65, v64, s[40:41]
	v_div_scale_f32 v65, s[12:13], v64, v64, 1.0
	v_fma_f32 v69, -v67, v68, 1.0
	v_fmac_f32_e32 v68, v69, v68
	v_div_scale_f32 v69, vcc, 1.0, v66, 1.0
	v_mul_f32_e32 v70, v69, v68
	v_fma_f32 v71, -v67, v70, v69
	v_fmac_f32_e32 v70, v71, v68
	v_fma_f32 v67, -v67, v70, v69
	v_div_fmas_f32 v67, v67, v68, v70
	v_div_fixup_f32 v66, v67, v66, 1.0
	v_rcp_f32_e32 v67, v65
	v_readlane_b32 s70, v255, 14
	s_mov_b32 s21, s20
	s_mov_b32 s71, s66
	v_fma_f32 v68, -v65, v67, 1.0
	v_fmac_f32_e32 v67, v68, v67
	v_div_scale_f32 v68, vcc, 1.0, v64, 1.0
	v_mul_f32_e32 v69, v68, v67
	v_fma_f32 v70, -v65, v69, v68
	v_fmac_f32_e32 v69, v70, v67
	v_fma_f32 v65, -v65, v69, v68
	v_div_fmas_f32 v65, v65, v67, v69
	v_div_fixup_f32 v64, v65, v64, 1.0
	v_pk_mul_f32 v[48:49], v[48:49], v[66:67] op_sel_hi:[1,0]
	v_pk_mul_f32 v[50:51], v[50:51], v[66:67] op_sel_hi:[1,0]
	v_pk_mul_f32 v[32:33], v[32:33], v[66:67] op_sel_hi:[1,0]
	v_pk_mul_f32 v[34:35], v[34:35], v[66:67] op_sel_hi:[1,0]
	v_pk_mul_f32 v[16:17], v[16:17], v[64:65] op_sel_hi:[1,0]
	v_pk_mul_f32 v[18:19], v[18:19], v[64:65] op_sel_hi:[1,0]
	v_pk_mul_f32 v[0:1], v[0:1], v[64:65] op_sel_hi:[1,0]
	v_pk_mul_f32 v[2:3], v[2:3], v[64:65] op_sel_hi:[1,0]
	v_cvt_pk_bf16_f32 v48, v48, v49
	v_cvt_pk_bf16_f32 v49, v50, v51
	v_lshl_add_u64 v[50:51], v[182:183], 1, v[192:193]
	v_cvt_pk_bf16_f32 v32, v32, v33
	v_cvt_pk_bf16_f32 v33, v34, v35
	v_cvt_pk_bf16_f32 v16, v16, v17
	v_cvt_pk_bf16_f32 v17, v18, v19
	v_cvt_pk_bf16_f32 v0, v0, v1
	v_cvt_pk_bf16_f32 v1, v2, v3
	global_store_dwordx2 v[50:51], v[48:49], off
	v_pk_mul_f32 v[48:49], v[52:53], v[66:67] op_sel_hi:[1,0]
	v_pk_mul_f32 v[52:53], v[54:55], v[66:67] op_sel_hi:[1,0]
	global_store_dwordx2 v[50:51], v[32:33], off offset:64
	v_pk_mul_f32 v[32:33], v[36:37], v[66:67] op_sel_hi:[1,0]
	v_pk_mul_f32 v[34:35], v[38:39], v[66:67] op_sel_hi:[1,0]
	global_store_dwordx2 v[50:51], v[16:17], off offset:128
	v_pk_mul_f32 v[16:17], v[20:21], v[64:65] op_sel_hi:[1,0]
	v_pk_mul_f32 v[18:19], v[22:23], v[64:65] op_sel_hi:[1,0]
	global_store_dwordx2 v[50:51], v[0:1], off offset:192
	v_pk_mul_f32 v[0:1], v[4:5], v[64:65] op_sel_hi:[1,0]
	v_pk_mul_f32 v[2:3], v[6:7], v[64:65] op_sel_hi:[1,0]
	v_cvt_pk_bf16_f32 v48, v48, v49
	v_cvt_pk_bf16_f32 v49, v52, v53
	v_cvt_pk_bf16_f32 v32, v32, v33
	v_cvt_pk_bf16_f32 v33, v34, v35
	v_cvt_pk_bf16_f32 v16, v16, v17
	v_cvt_pk_bf16_f32 v17, v18, v19
	v_cvt_pk_bf16_f32 v0, v0, v1
	v_cvt_pk_bf16_f32 v1, v2, v3
	global_store_dwordx2 v[50:51], v[48:49], off offset:16
	v_pk_mul_f32 v[48:49], v[56:57], v[66:67] op_sel_hi:[1,0]
	v_pk_mul_f32 v[52:53], v[58:59], v[66:67] op_sel_hi:[1,0]
	global_store_dwordx2 v[50:51], v[32:33], off offset:80
	v_pk_mul_f32 v[32:33], v[40:41], v[66:67] op_sel_hi:[1,0]
	v_pk_mul_f32 v[34:35], v[42:43], v[66:67] op_sel_hi:[1,0]
	global_store_dwordx2 v[50:51], v[16:17], off offset:144
	v_pk_mul_f32 v[16:17], v[24:25], v[64:65] op_sel_hi:[1,0]
	v_pk_mul_f32 v[18:19], v[26:27], v[64:65] op_sel_hi:[1,0]
	global_store_dwordx2 v[50:51], v[0:1], off offset:208
	v_pk_mul_f32 v[0:1], v[8:9], v[64:65] op_sel_hi:[1,0]
	v_pk_mul_f32 v[2:3], v[10:11], v[64:65] op_sel_hi:[1,0]
	v_cvt_pk_bf16_f32 v48, v48, v49
	v_cvt_pk_bf16_f32 v49, v52, v53
	v_cvt_pk_bf16_f32 v32, v32, v33
	v_cvt_pk_bf16_f32 v33, v34, v35
	v_cvt_pk_bf16_f32 v16, v16, v17
	v_cvt_pk_bf16_f32 v17, v18, v19
	v_cvt_pk_bf16_f32 v0, v0, v1
	v_cvt_pk_bf16_f32 v1, v2, v3
	global_store_dwordx2 v[50:51], v[48:49], off offset:32
	v_pk_mul_f32 v[48:49], v[60:61], v[66:67] op_sel_hi:[1,0]
	v_pk_mul_f32 v[52:53], v[62:63], v[66:67] op_sel_hi:[1,0]
	global_store_dwordx2 v[50:51], v[32:33], off offset:96
	v_pk_mul_f32 v[32:33], v[44:45], v[66:67] op_sel_hi:[1,0]
	v_pk_mul_f32 v[34:35], v[46:47], v[66:67] op_sel_hi:[1,0]
	global_store_dwordx2 v[50:51], v[16:17], off offset:160
	v_pk_mul_f32 v[16:17], v[28:29], v[64:65] op_sel_hi:[1,0]
	v_pk_mul_f32 v[18:19], v[30:31], v[64:65] op_sel_hi:[1,0]
	global_store_dwordx2 v[50:51], v[0:1], off offset:224
	v_pk_mul_f32 v[0:1], v[12:13], v[64:65] op_sel_hi:[1,0]
	v_cvt_pk_bf16_f32 v48, v48, v49
	v_cvt_pk_bf16_f32 v49, v52, v53
	v_cvt_pk_bf16_f32 v32, v32, v33
	v_cvt_pk_bf16_f32 v33, v34, v35
	v_cvt_pk_bf16_f32 v16, v16, v17
	v_cvt_pk_bf16_f32 v17, v18, v19
	v_cvt_pk_bf16_f32 v0, v0, v1
	v_pk_mul_f32 v[2:3], v[14:15], v[64:65] op_sel_hi:[1,0]
	global_store_dwordx2 v[50:51], v[48:49], off offset:48
	global_store_dwordx2 v[50:51], v[32:33], off offset:112
	global_store_dwordx2 v[50:51], v[16:17], off offset:176

.LBB0_642:
	s_bitcmp1_b32 s2, 0
	s_mov_b32 s14, 0x2200000
	s_cselect_b32 s13, 0, 0x5400
	v_add_co_u32_e32 v64, vcc, s14, v152
	s_cselect_b32 s12, 0x5400, 0
	global_load_dwordx4 v[142:145], v[152:153], off
	v_addc_co_u32_e32 v65, vcc, 0, v153, vcc
	global_load_dwordx4 v[146:149], v[64:65], off
	v_add3_u32 v206, s13, v220, v223
	ds_read_b128 v[80:83], v206
	ds_read_b128 v[84:87], v206 offset:32
	ds_read_b128 v[154:157], v206 offset:64
	ds_read_b128 v[158:161], v206 offset:96
	s_waitcnt lgkmcnt(0)
	v_add_u32_e32 v112, s13, v221
	v_mfma_f32_32x32x16_bf16 v[96:111], v[80:83], v[126:129], 0.5
	v_add3_u32 v112, v112, v222, v224
	s_add_i32 s2, s2, 1
	s_add_i32 s13, s4, s2
	v_lshl_add_u64 v[152:153], v[152:153], 0, s[84:85]
	s_cmp_eq_u32 s13, 2
	v_mfma_f32_32x32x16_bf16 v[96:111], v[84:87], v[130:133], v[96:111]
	v_mfma_f32_32x32x16_bf16 v[80:95], v[154:157], v[118:121], 0.5
	s_nop 10
	v_cvt_pknorm_i16_f32 v96, v96, v97
	v_cvt_pknorm_i16_f32 v97, v98, v99
	v_cvt_pknorm_i16_f32 v98, v100, v101
	v_cvt_pknorm_i16_f32 v99, v102, v103
	v_cvt_pknorm_i16_f32 v104, v104, v105
	v_cvt_pknorm_i16_f32 v105, v106, v107
	v_cvt_pknorm_i16_f32 v106, v108, v109
	v_mfma_f32_32x32x16_bf16 v[80:95], v[158:161], v[122:125], v[80:95]
	ds_read_b64_tr_b16 v[154:155], v112 offset:9216
	ds_read_b64_tr_b16 v[156:157], v112 offset:10752
	ds_read_b64_tr_b16 v[158:159], v112 offset:12288
	ds_read_b64_tr_b16 v[160:161], v112 offset:13824
	ds_read_b64_tr_b16 v[162:163], v112 offset:9280
	ds_read_b64_tr_b16 v[164:165], v112 offset:10816
	ds_read_b64_tr_b16 v[192:193], v112 offset:12352
	ds_read_b64_tr_b16 v[194:195], v112 offset:13888
	v_cvt_pknorm_i16_f32 v107, v110, v111
	s_nop 2
	v_cvt_pknorm_i16_f32 v80, v80, v81
	v_cvt_pknorm_i16_f32 v81, v82, v83
	v_cvt_pknorm_i16_f32 v82, v84, v85
	v_cvt_pknorm_i16_f32 v83, v86, v87
	s_waitcnt lgkmcnt(6)
	v_mfma_f32_32x32x16_bf16 v[32:47], v[154:157], v[96:99], v[32:47]
	v_cvt_pknorm_i16_f32 v88, v88, v89
	v_cvt_pknorm_i16_f32 v89, v90, v91
	v_cvt_pknorm_i16_f32 v90, v92, v93
	v_cvt_pknorm_i16_f32 v91, v94, v95
	v_mfma_f32_32x32x16_bf16 v[48:63], v[154:157], v[80:83], v[48:63]
	s_waitcnt lgkmcnt(2)
	v_mfma_f32_32x32x16_bf16 v[0:15], v[162:165], v[96:99], v[0:15]
	v_mfma_f32_16x16x32_bf16 v[84:87], v[114:117], v[80:83], v[138:141]
	v_mfma_f32_16x16x32_bf16 v[100:103], v[114:117], v[96:99], v[134:137]
	v_mfma_f32_32x32x16_bf16 v[32:47], v[158:161], v[104:107], v[32:47]
	v_mfma_f32_16x16x32_bf16 v[138:141], v[114:117], v[88:91], v[84:87]
	v_mfma_f32_32x32x16_bf16 v[48:63], v[158:161], v[88:91], v[48:63]
	v_mfma_f32_32x32x16_bf16 v[16:31], v[162:165], v[80:83], v[16:31]
	ds_read_b128 v[80:83], v206 offset:4608
	s_nop 1
	ds_read_b128 v[84:87], v206 offset:4640
	ds_read_b128 v[154:157], v206 offset:4672
	ds_read_b128 v[158:161], v206 offset:4704
	s_waitcnt lgkmcnt(0)
	v_mfma_f32_16x16x32_bf16 v[134:137], v[114:117], v[104:107], v[100:103]
	v_mfma_f32_32x32x16_bf16 v[0:15], v[192:195], v[104:107], v[0:15]
	v_mfma_f32_32x32x16_bf16 v[96:111], v[80:83], v[126:129], 0.5
	v_mfma_f32_32x32x16_bf16 v[16:31], v[192:195], v[88:91], v[16:31]
	v_mfma_f32_32x32x16_bf16 v[96:111], v[84:87], v[130:133], v[96:111]
	v_mfma_f32_32x32x16_bf16 v[80:95], v[154:157], v[118:121], 0.5
	ds_read_b64_tr_b16 v[64:65], v112 offset:15360
	ds_read_b64_tr_b16 v[66:67], v112 offset:16896
	ds_read_b64_tr_b16 v[68:69], v112 offset:18432
	ds_read_b64_tr_b16 v[70:71], v112 offset:19968
	ds_read_b64_tr_b16 v[72:73], v112 offset:15424
	ds_read_b64_tr_b16 v[74:75], v112 offset:16960
	ds_read_b64_tr_b16 v[76:77], v112 offset:18496
	ds_read_b64_tr_b16 v[78:79], v112 offset:20032
	v_cvt_pknorm_i16_f32 v96, v96, v97
	v_cvt_pknorm_i16_f32 v97, v98, v99
	v_cvt_pknorm_i16_f32 v98, v100, v101
	v_cvt_pknorm_i16_f32 v99, v102, v103
	v_cvt_pknorm_i16_f32 v104, v104, v105
	v_cvt_pknorm_i16_f32 v105, v106, v107
	v_mfma_f32_32x32x16_bf16 v[80:95], v[158:161], v[122:125], v[80:95]
	v_cvt_pknorm_i16_f32 v106, v108, v109
	v_cvt_pknorm_i16_f32 v107, v110, v111
	s_waitcnt lgkmcnt(6)
	v_mfma_f32_32x32x16_bf16 v[32:47], v[64:67], v[96:99], v[32:47]
	s_nop 7
	v_cvt_pknorm_i16_f32 v80, v80, v81
	v_cvt_pknorm_i16_f32 v81, v82, v83
	v_cvt_pknorm_i16_f32 v82, v84, v85
	v_cvt_pknorm_i16_f32 v83, v86, v87
	v_cvt_pknorm_i16_f32 v88, v88, v89
	v_cvt_pknorm_i16_f32 v89, v90, v91
	v_cvt_pknorm_i16_f32 v90, v92, v93
	s_waitcnt lgkmcnt(2)
	v_mfma_f32_32x32x16_bf16 v[0:15], v[72:75], v[96:99], v[0:15]
	v_cvt_pknorm_i16_f32 v91, v94, v95
	v_mfma_f32_32x32x16_bf16 v[48:63], v[64:67], v[80:83], v[48:63]
	v_add3_u32 v64, s12, v217, v218
	v_add3_u32 v65, s12, v219, v218
	s_waitcnt vmcnt(1)
	ds_write_b128 v64, v[142:145]
	s_waitcnt vmcnt(0)
	ds_write_b128 v65, v[146:149] offset:9216
	s_waitcnt lgkmcnt(0)
	s_barrier
	v_mfma_f32_32x32x16_bf16 v[16:31], v[72:75], v[80:83], v[16:31]
	v_mfma_f32_16x16x32_bf16 v[100:103], v[114:117], v[96:99], v[134:137]
	v_mfma_f32_32x32x16_bf16 v[32:47], v[68:71], v[104:107], v[32:47]
	v_mfma_f32_32x32x16_bf16 v[0:15], v[76:79], v[104:107], v[0:15]
	v_mfma_f32_16x16x32_bf16 v[84:87], v[114:117], v[80:83], v[138:141]
	v_mfma_f32_32x32x16_bf16 v[48:63], v[68:71], v[88:91], v[48:63]
	v_mfma_f32_32x32x16_bf16 v[16:31], v[76:79], v[88:91], v[16:31]
	v_mfma_f32_16x16x32_bf16 v[134:137], v[114:117], v[104:107], v[100:103]
	v_mfma_f32_16x16x32_bf16 v[138:141], v[114:117], v[88:91], v[84:87]
	s_cbranch_scc0 .LBB0_642
	v_add3_u32 v112, s12, v220, v223
	v_mov_b64_e32 v[64:65], s[68:69]
	ds_read_b128 v[80:83], v112
	v_mov_b64_e32 v[66:67], s[70:71]
	v_mov_b64_e32 v[68:69], s[72:73]
	v_mov_b64_e32 v[70:71], s[74:75]
	v_mov_b64_e32 v[72:73], s[76:77]
	v_mov_b64_e32 v[74:75], s[78:79]
	v_mov_b64_e32 v[76:77], s[80:81]
	v_mov_b64_e32 v[78:79], s[82:83]
	ds_read_b128 v[84:87], v112 offset:32
	ds_read_b128 v[142:145], v112 offset:64
	ds_read_b128 v[146:149], v112 offset:96
	s_waitcnt lgkmcnt(3)
	s_waitcnt lgkmcnt(2)
	v_mfma_f32_32x32x16_bf16 v[96:111], v[80:83], v[126:129], v[64:79]
	s_waitcnt lgkmcnt(1)
	s_waitcnt lgkmcnt(0)
	v_mfma_f32_32x32x16_bf16 v[96:111], v[84:87], v[130:133], v[96:111]
	v_mfma_f32_32x32x16_bf16 v[80:95], v[142:145], v[118:121], v[64:79]
	v_add_u32_e32 v142, s12, v221
	v_add3_u32 v160, v142, v222, v224
	ds_read_b64_tr_b16 v[142:143], v160 offset:9216
	ds_read_b64_tr_b16 v[144:145], v160 offset:10752
	s_nop 6
	v_cvt_pknorm_i16_f32 v96, v96, v97
	v_cvt_pknorm_i16_f32 v97, v98, v99
	v_cvt_pknorm_i16_f32 v98, v100, v101
	v_cvt_pknorm_i16_f32 v99, v102, v103
	v_mfma_f32_32x32x16_bf16 v[80:95], v[146:149], v[122:125], v[80:95]
	ds_read_b64_tr_b16 v[102:103], v160 offset:10816
	ds_read_b64_tr_b16 v[100:101], v160 offset:9280
	ds_read_b64_tr_b16 v[146:147], v160 offset:12288
	ds_read_b64_tr_b16 v[148:149], v160 offset:13824
	v_cvt_pknorm_i16_f32 v104, v104, v105
	v_cvt_pknorm_i16_f32 v105, v106, v107
	v_cvt_pknorm_i16_f32 v106, v108, v109
	v_cvt_pknorm_i16_f32 v107, v110, v111
	ds_read_b64_tr_b16 v[110:111], v160 offset:13888
	ds_read_b64_tr_b16 v[108:109], v160 offset:12352
	s_nop 1
	v_cvt_pknorm_i16_f32 v152, v80, v81
	v_cvt_pknorm_i16_f32 v153, v82, v83
	v_cvt_pknorm_i16_f32 v154, v84, v85
	v_cvt_pknorm_i16_f32 v155, v86, v87
	s_waitcnt lgkmcnt(6)
	v_mfma_f32_32x32x16_bf16 v[32:47], v[142:145], v[96:99], v[32:47]
	s_waitcnt lgkmcnt(4)
	v_mfma_f32_32x32x16_bf16 v[0:15], v[100:103], v[96:99], v[0:15]
	v_mfma_f32_32x32x16_bf16 v[48:63], v[142:145], v[152:155], v[48:63]
	v_cvt_pknorm_i16_f32 v142, v88, v89
	v_cvt_pknorm_i16_f32 v143, v90, v91
	v_cvt_pknorm_i16_f32 v144, v92, v93
	v_cvt_pknorm_i16_f32 v145, v94, v95
	v_mfma_f32_32x32x16_bf16 v[16:31], v[100:103], v[152:155], v[16:31]
	s_waitcnt lgkmcnt(2)
	v_mfma_f32_32x32x16_bf16 v[32:47], v[146:149], v[104:107], v[32:47]
	s_waitcnt lgkmcnt(0)
	v_mfma_f32_32x32x16_bf16 v[0:15], v[108:111], v[104:107], v[0:15]
	v_mfma_f32_32x32x16_bf16 v[48:63], v[146:149], v[142:145], v[48:63]
	v_mfma_f32_32x32x16_bf16 v[16:31], v[108:111], v[142:145], v[16:31]
	ds_read_b128 v[100:103], v112 offset:4608
	ds_read_b128 v[108:111], v112 offset:4640
	ds_read_b128 v[146:149], v112 offset:4672
	ds_read_b128 v[156:159], v112 offset:4704
	s_waitcnt lgkmcnt(3)
	s_waitcnt lgkmcnt(2)
	s_waitcnt lgkmcnt(1)
	s_waitcnt lgkmcnt(0)
	v_mfma_f32_32x32x16_bf16 v[80:95], v[100:103], v[126:129], v[64:79]
	ds_read_b64_tr_b16 v[100:101], v160 offset:15360
	ds_read_b64_tr_b16 v[102:103], v160 offset:16896
	v_mfma_f32_32x32x16_bf16 v[80:95], v[108:111], v[130:133], v[80:95]
	v_mfma_f32_32x32x16_bf16 v[64:79], v[146:149], v[118:121], v[64:79]
	s_nop 10
	v_cvt_pknorm_i16_f32 v80, v80, v81
	v_cvt_pknorm_i16_f32 v81, v82, v83
	v_cvt_pknorm_i16_f32 v82, v84, v85
	v_cvt_pknorm_i16_f32 v83, v86, v87
	ds_read_b64_tr_b16 v[86:87], v160 offset:16960
	ds_read_b64_tr_b16 v[84:85], v160 offset:15424
	ds_read_b64_tr_b16 v[108:109], v160 offset:18432
	ds_read_b64_tr_b16 v[110:111], v160 offset:19968
	v_cvt_pknorm_i16_f32 v88, v88, v89
	v_mfma_f32_32x32x16_bf16 v[64:79], v[156:159], v[122:125], v[64:79]
	v_cvt_pknorm_i16_f32 v89, v90, v91
	v_cvt_pknorm_i16_f32 v90, v92, v93
	v_cvt_pknorm_i16_f32 v91, v94, v95
	ds_read_b64_tr_b16 v[94:95], v160 offset:20032
	ds_read_b64_tr_b16 v[92:93], v160 offset:18496
	s_load_dword s2, s[6:7], 0x180
	s_waitcnt lgkmcnt(0)
	s_barrier
	v_mfma_f32_32x32x16_bf16 v[0:15], v[84:87], v[80:83], v[0:15]
	s_nop 2
	v_cvt_pknorm_i16_f32 v64, v64, v65
	v_cvt_pknorm_i16_f32 v65, v66, v67
	v_cvt_pknorm_i16_f32 v66, v68, v69
	v_cvt_pknorm_i16_f32 v68, v72, v73
	v_cvt_pknorm_i16_f32 v69, v74, v75
	v_cvt_pknorm_i16_f32 v67, v70, v71
	v_cvt_pknorm_i16_f32 v70, v76, v77
	v_mfma_f32_16x16x32_bf16 v[72:75], v[114:117], v[96:99], v[134:137]
	v_cvt_pknorm_i16_f32 v71, v78, v79
	v_mfma_f32_16x16x32_bf16 v[76:79], v[114:117], v[152:155], v[138:141]
	v_mfma_f32_16x16x32_bf16 v[72:75], v[114:117], v[104:107], v[72:75]
	v_mfma_f32_32x32x16_bf16 v[32:47], v[100:103], v[80:83], v[32:47]
	v_mfma_f32_32x32x16_bf16 v[0:15], v[92:95], v[88:91], v[0:15]
	v_mfma_f32_32x32x16_bf16 v[48:63], v[100:103], v[64:67], v[48:63]
	v_mfma_f32_32x32x16_bf16 v[16:31], v[84:87], v[64:67], v[16:31]
	v_mfma_f32_16x16x32_bf16 v[76:79], v[114:117], v[142:145], v[76:79]
	v_mfma_f32_16x16x32_bf16 v[72:75], v[114:117], v[80:83], v[72:75]
	v_mfma_f32_16x16x32_bf16 v[64:67], v[114:117], v[64:67], v[76:79]
	v_mfma_f32_16x16x32_bf16 v[72:75], v[114:117], v[88:91], v[72:75]
	v_mfma_f32_32x32x16_bf16 v[32:47], v[108:111], v[88:91], v[32:47]
	s_nop 6
	v_sub_f32_e64 v74, 1.0, s2
	v_mfma_f32_32x32x16_bf16 v[48:63], v[108:111], v[68:71], v[48:63]
	v_mfma_f32_16x16x32_bf16 v[64:67], v[114:117], v[68:71], v[64:67]
	v_mfma_f32_32x32x16_bf16 v[16:31], v[92:95], v[68:71], v[16:31]
	s_setprio 0
	s_nop 5
	ds_bpermute_b32 v66, v181, v72
	ds_bpermute_b32 v67, v181, v73
	ds_bpermute_b32 v64, v181, v64
	ds_bpermute_b32 v65, v181, v65
	v_readlane_b32 s70, v255, 14
	s_mov_b32 s21, s20
	s_waitcnt lgkmcnt(2)
	v_cndmask_b32_e64 v66, v67, v66, s[40:41]
	v_div_scale_f32 v67, s[12:13], v66, v66, 1.0
	v_rcp_f32_e32 v68, v67
	s_waitcnt lgkmcnt(0)
	v_cndmask_b32_e64 v64, v65, v64, s[40:41]
	v_div_scale_f32 v65, s[12:13], v64, v64, 1.0
	v_fma_f32 v69, -v67, v68, 1.0
	v_fmac_f32_e32 v68, v69, v68
	v_div_scale_f32 v69, vcc, 1.0, v66, 1.0
	v_mul_f32_e32 v70, v69, v68
	v_fma_f32 v71, -v67, v70, v69
	v_fmac_f32_e32 v70, v71, v68
	v_fma_f32 v67, -v67, v70, v69
	v_div_fmas_f32 v67, v67, v68, v70
	v_div_fixup_f32 v66, v67, v66, 1.0
	v_rcp_f32_e32 v67, v65
	s_mov_b32 s71, s66
	v_fma_f32 v68, -v65, v67, 1.0
	v_fmac_f32_e32 v67, v68, v67
	v_div_scale_f32 v68, vcc, 1.0, v64, 1.0
	v_mul_f32_e32 v69, v68, v67
	v_fma_f32 v70, -v65, v69, v68
	v_fmac_f32_e32 v69, v70, v67
	v_fma_f32 v65, -v65, v69, v68
	v_div_fmas_f32 v65, v65, v67, v69
	global_load_dwordx4 v[68:71], v[186:187], off
	v_div_fixup_f32 v72, v65, v64, 1.0
	v_pk_mul_f32 v[30:31], v[30:31], v[72:73] op_sel_hi:[1,0]
	v_pk_mul_f32 v[18:19], v[18:19], v[72:73] op_sel_hi:[1,0]
	v_pk_mul_f32 v[30:31], v[166:167], v[30:31]
	v_pk_mul_f32 v[18:19], v[166:167], v[18:19]
	v_pk_fma_f32 v[14:15], v[14:15], v[66:67], v[30:31] op_sel_hi:[1,0,1] neg_lo:[0,0,1] neg_hi:[0,0,1]
	v_pk_mul_f32 v[30:31], v[50:51], v[72:73] op_sel_hi:[1,0]
	v_pk_fma_f32 v[18:19], v[2:3], v[66:67], v[18:19] op_sel_hi:[1,0,1] neg_lo:[0,0,1] neg_hi:[0,0,1]
	v_pk_mul_f32 v[30:31], v[166:167], v[30:31]
	v_pk_mul_f32 v[2:3], v[16:17], v[72:73] op_sel_hi:[1,0]
	v_pk_fma_f32 v[30:31], v[34:35], v[66:67], v[30:31] op_sel_hi:[1,0,1] neg_lo:[0,0,1] neg_hi:[0,0,1]
	v_pk_mul_f32 v[34:35], v[48:49], v[72:73] op_sel_hi:[1,0]
	v_mul_f32_e32 v48, v31, v31
	v_pk_mul_f32 v[34:35], v[166:167], v[34:35]
	v_pk_mul_f32 v[2:3], v[166:167], v[2:3]
	v_pk_fma_f32 v[32:33], v[32:33], v[66:67], v[34:35] op_sel_hi:[1,0,1] neg_lo:[0,0,1] neg_hi:[0,0,1]
	v_pk_fma_f32 v[16:17], v[0:1], v[66:67], v[2:3] op_sel_hi:[1,0,1] neg_lo:[0,0,1] neg_hi:[0,0,1]
	v_mul_f32_e32 v34, v33, v33
	v_pk_fma_f32 v[34:35], v[32:33], v[32:33], v[34:35] op_sel_hi:[1,1,0]
	v_mul_f32_e32 v2, v17, v17
	v_pk_fma_f32 v[34:35], v[30:31], v[30:31], v[34:35]
	v_lshl_add_u64 v[64:65], v[182:183], 1, v[150:151]
	v_pk_add_f32 v[34:35], v[48:49], v[34:35] op_sel_hi:[0,1]
	v_pk_mul_f32 v[48:49], v[54:55], v[72:73] op_sel_hi:[1,0]
	s_nop 0
	v_pk_mul_f32 v[48:49], v[166:167], v[48:49]
	s_nop 0
	v_pk_fma_f32 v[38:39], v[38:39], v[66:67], v[48:49] op_sel_hi:[1,0,1] neg_lo:[0,0,1] neg_hi:[0,0,1]
	v_pk_mul_f32 v[48:49], v[52:53], v[72:73] op_sel_hi:[1,0]
	s_nop 0
	v_pk_mul_f32 v[48:49], v[166:167], v[48:49]
	s_nop 0
	v_pk_fma_f32 v[36:37], v[36:37], v[66:67], v[48:49] op_sel_hi:[1,0,1] neg_lo:[0,0,1] neg_hi:[0,0,1]
	s_nop 0
	v_pk_fma_f32 v[34:35], v[36:37], v[36:37], v[34:35]
	v_mul_f32_e32 v48, v37, v37
	v_pk_add_f32 v[34:35], v[48:49], v[34:35] op_sel_hi:[0,1]
	v_pk_fma_f32 v[34:35], v[38:39], v[38:39], v[34:35]
	v_mul_f32_e32 v48, v39, v39
	v_pk_add_f32 v[34:35], v[48:49], v[34:35] op_sel_hi:[0,1]
	v_pk_mul_f32 v[48:49], v[58:59], v[72:73] op_sel_hi:[1,0]
	s_nop 0
	v_pk_mul_f32 v[48:49], v[166:167], v[48:49]
	s_nop 0
	v_pk_fma_f32 v[42:43], v[42:43], v[66:67], v[48:49] op_sel_hi:[1,0,1] neg_lo:[0,0,1] neg_hi:[0,0,1]
	v_pk_mul_f32 v[48:49], v[56:57], v[72:73] op_sel_hi:[1,0]
	s_nop 0
	v_pk_mul_f32 v[48:49], v[166:167], v[48:49]
	s_nop 0
	v_pk_fma_f32 v[40:41], v[40:41], v[66:67], v[48:49] op_sel_hi:[1,0,1] neg_lo:[0,0,1] neg_hi:[0,0,1]
	s_nop 0
	v_pk_fma_f32 v[34:35], v[40:41], v[40:41], v[34:35]
	v_mul_f32_e32 v48, v41, v41
	v_pk_add_f32 v[34:35], v[48:49], v[34:35] op_sel_hi:[0,1]
	v_pk_fma_f32 v[34:35], v[42:43], v[42:43], v[34:35]
	v_mul_f32_e32 v48, v43, v43
	v_pk_add_f32 v[34:35], v[48:49], v[34:35] op_sel_hi:[0,1]
	v_pk_mul_f32 v[48:49], v[62:63], v[72:73] op_sel_hi:[1,0]
	s_nop 0
	v_pk_mul_f32 v[48:49], v[166:167], v[48:49]
	s_nop 0
	v_pk_fma_f32 v[46:47], v[46:47], v[66:67], v[48:49] op_sel_hi:[1,0,1] neg_lo:[0,0,1] neg_hi:[0,0,1]
	v_pk_mul_f32 v[48:49], v[60:61], v[72:73] op_sel_hi:[1,0]
	s_nop 0
	v_pk_mul_f32 v[48:49], v[166:167], v[48:49]
	s_nop 0
	v_pk_fma_f32 v[44:45], v[44:45], v[66:67], v[48:49] op_sel_hi:[1,0,1] neg_lo:[0,0,1] neg_hi:[0,0,1]
	s_nop 0
	v_pk_fma_f32 v[34:35], v[44:45], v[44:45], v[34:35]
	v_mul_f32_e32 v48, v45, v45
	v_pk_add_f32 v[34:35], v[48:49], v[34:35] op_sel_hi:[0,1]
	v_pk_fma_f32 v[34:35], v[46:47], v[46:47], v[34:35]
	v_mul_f32_e32 v48, v47, v47
	v_pk_add_f32 v[34:35], v[48:49], v[34:35] op_sel_hi:[0,1]
	v_pk_fma_f32 v[0:1], v[16:17], v[16:17], v[34:35]
	s_nop 0
	v_pk_add_f32 v[0:1], v[2:3], v[0:1] op_sel_hi:[0,1]
	v_pk_fma_f32 v[0:1], v[18:19], v[18:19], v[0:1]
	v_mul_f32_e32 v2, v19, v19
	v_pk_add_f32 v[0:1], v[2:3], v[0:1] op_sel_hi:[0,1]
	v_pk_mul_f32 v[2:3], v[22:23], v[72:73] op_sel_hi:[1,0]
	s_nop 0
	v_pk_mul_f32 v[2:3], v[166:167], v[2:3]
	s_nop 0
	v_pk_fma_f32 v[6:7], v[6:7], v[66:67], v[2:3] op_sel_hi:[1,0,1] neg_lo:[0,0,1] neg_hi:[0,0,1]
	v_pk_mul_f32 v[2:3], v[20:21], v[72:73] op_sel_hi:[1,0]
	s_nop 0
	v_pk_mul_f32 v[2:3], v[166:167], v[2:3]
	s_nop 0
	v_pk_fma_f32 v[4:5], v[4:5], v[66:67], v[2:3] op_sel_hi:[1,0,1] neg_lo:[0,0,1] neg_hi:[0,0,1]
	s_nop 0
	v_pk_fma_f32 v[0:1], v[4:5], v[4:5], v[0:1]
	v_mul_f32_e32 v2, v5, v5
	v_pk_add_f32 v[0:1], v[2:3], v[0:1] op_sel_hi:[0,1]
	v_pk_fma_f32 v[0:1], v[6:7], v[6:7], v[0:1]
	v_mul_f32_e32 v2, v7, v7
	v_pk_add_f32 v[0:1], v[2:3], v[0:1] op_sel_hi:[0,1]
	v_pk_mul_f32 v[2:3], v[26:27], v[72:73] op_sel_hi:[1,0]
	s_nop 0
	v_pk_mul_f32 v[2:3], v[166:167], v[2:3]
	s_nop 0
	v_pk_fma_f32 v[10:11], v[10:11], v[66:67], v[2:3] op_sel_hi:[1,0,1] neg_lo:[0,0,1] neg_hi:[0,0,1]
	v_pk_mul_f32 v[2:3], v[24:25], v[72:73] op_sel_hi:[1,0]
	s_nop 0
	v_pk_mul_f32 v[2:3], v[166:167], v[2:3]
	s_nop 0
	v_pk_fma_f32 v[8:9], v[8:9], v[66:67], v[2:3] op_sel_hi:[1,0,1] neg_lo:[0,0,1] neg_hi:[0,0,1]
	s_nop 0
	v_pk_fma_f32 v[0:1], v[8:9], v[8:9], v[0:1]
	v_mul_f32_e32 v2, v9, v9
	v_pk_add_f32 v[0:1], v[2:3], v[0:1] op_sel_hi:[0,1]
	v_pk_fma_f32 v[0:1], v[10:11], v[10:11], v[0:1]
	v_mul_f32_e32 v2, v11, v11
	v_pk_add_f32 v[0:1], v[2:3], v[0:1] op_sel_hi:[0,1]
	v_pk_mul_f32 v[2:3], v[28:29], v[72:73] op_sel_hi:[1,0]
	s_nop 0
	v_pk_mul_f32 v[2:3], v[166:167], v[2:3]
	s_nop 0
	v_pk_fma_f32 v[12:13], v[12:13], v[66:67], v[2:3] op_sel_hi:[1,0,1] neg_lo:[0,0,1] neg_hi:[0,0,1]
	s_nop 0
	v_pk_fma_f32 v[0:1], v[12:13], v[12:13], v[0:1]
	v_mul_f32_e32 v2, v13, v13
	v_pk_add_f32 v[0:1], v[2:3], v[0:1] op_sel_hi:[0,1]
	v_pk_fma_f32 v[0:1], v[14:15], v[14:15], v[0:1]
	v_mul_f32_e32 v2, v15, v15
	v_pk_add_f32 v[0:1], v[2:3], v[0:1] op_sel_hi:[0,1]
	v_mov_b32_e32 v1, v0
	s_nop 1
	v_permlane32_swap_b32_e32 v0, v1
	v_add_f32_e32 v0, v0, v1
	v_fmamk_f32 v0, v0, 0x3c800000, v196
	v_cmp_gt_f32_e32 vcc, s35, v0
	v_mul_f32_e32 v1, 0x4b800000, v0
	s_nop 0
	v_cndmask_b32_e32 v0, v0, v1, vcc
	v_rsq_f32_e32 v0, v0
	s_nop 0
	v_mul_f32_e32 v1, 0x45800000, v0
	v_cndmask_b32_e32 v0, v0, v1, vcc
	v_mul_f32_e32 v20, v74, v0
	v_pk_mul_f32 v[0:1], v[32:33], v[20:21] op_sel_hi:[1,0]
	v_pk_mul_f32 v[2:3], v[30:31], v[20:21] op_sel_hi:[1,0]
	s_waitcnt vmcnt(0)
	v_pk_mul_f32 v[0:1], v[68:69], v[0:1]
	v_pk_mul_f32 v[2:3], v[70:71], v[2:3]
	v_cvt_pk_bf16_f32 v0, v0, v1
	v_cvt_pk_bf16_f32 v1, v2, v3
	global_store_dwordx2 v[64:65], v[0:1], off
	global_load_dwordx4 v[0:3], v[186:187], off offset:32
	v_pk_mul_f32 v[22:23], v[36:37], v[20:21] op_sel_hi:[1,0]
	v_pk_mul_f32 v[16:17], v[16:17], v[20:21] op_sel_hi:[1,0]
	v_pk_mul_f32 v[4:5], v[4:5], v[20:21] op_sel_hi:[1,0]
	s_waitcnt vmcnt(0)
	v_pk_mul_f32 v[0:1], v[0:1], v[22:23]
	v_pk_mul_f32 v[22:23], v[38:39], v[20:21] op_sel_hi:[1,0]
	v_cvt_pk_bf16_f32 v0, v0, v1
	v_pk_mul_f32 v[2:3], v[2:3], v[22:23]
	v_pk_mul_f32 v[22:23], v[40:41], v[20:21] op_sel_hi:[1,0]
	v_cvt_pk_bf16_f32 v1, v2, v3
	global_store_dwordx2 v[64:65], v[0:1], off offset:16
	global_load_dwordx4 v[0:3], v[186:187], off offset:64
	s_waitcnt vmcnt(0)
	v_pk_mul_f32 v[0:1], v[0:1], v[22:23]
	v_pk_mul_f32 v[22:23], v[42:43], v[20:21] op_sel_hi:[1,0]
	v_cvt_pk_bf16_f32 v0, v0, v1
	v_pk_mul_f32 v[2:3], v[2:3], v[22:23]
	v_pk_mul_f32 v[22:23], v[44:45], v[20:21] op_sel_hi:[1,0]
	v_cvt_pk_bf16_f32 v1, v2, v3
	global_store_dwordx2 v[64:65], v[0:1], off offset:32
	global_load_dwordx4 v[0:3], v[186:187], off offset:96
	s_waitcnt vmcnt(0)
	v_pk_mul_f32 v[0:1], v[0:1], v[22:23]
	v_pk_mul_f32 v[22:23], v[46:47], v[20:21] op_sel_hi:[1,0]
	v_cvt_pk_bf16_f32 v0, v0, v1
	v_pk_mul_f32 v[2:3], v[2:3], v[22:23]
	s_nop 0
	v_cvt_pk_bf16_f32 v1, v2, v3
	global_store_dwordx2 v[64:65], v[0:1], off offset:48
	global_load_dwordx4 v[0:3], v[186:187], off offset:128
	s_waitcnt vmcnt(0)
	v_pk_mul_f32 v[0:1], v[0:1], v[16:17]
	v_pk_mul_f32 v[16:17], v[18:19], v[20:21] op_sel_hi:[1,0]
	v_cvt_pk_bf16_f32 v0, v0, v1
	v_pk_mul_f32 v[2:3], v[2:3], v[16:17]
	s_nop 0
	v_cvt_pk_bf16_f32 v1, v2, v3
	global_store_dwordx2 v[64:65], v[0:1], off offset:64
	global_load_dwordx4 v[0:3], v[186:187], off offset:160
	s_waitcnt vmcnt(0)
	v_pk_mul_f32 v[0:1], v[0:1], v[4:5]
	v_pk_mul_f32 v[4:5], v[6:7], v[20:21] op_sel_hi:[1,0]
	v_cvt_pk_bf16_f32 v0, v0, v1
	v_pk_mul_f32 v[2:3], v[2:3], v[4:5]
	v_pk_mul_f32 v[4:5], v[8:9], v[20:21] op_sel_hi:[1,0]
	v_cvt_pk_bf16_f32 v1, v2, v3
	global_store_dwordx2 v[64:65], v[0:1], off offset:80
	global_load_dwordx4 v[0:3], v[186:187], off offset:192
	s_waitcnt vmcnt(0)
	v_pk_mul_f32 v[0:1], v[4:5], v[0:1]
	v_pk_mul_f32 v[4:5], v[10:11], v[20:21] op_sel_hi:[1,0]
	v_cvt_pk_bf16_f32 v0, v0, v1
	v_pk_mul_f32 v[2:3], v[4:5], v[2:3]
	v_pk_mul_f32 v[4:5], v[12:13], v[20:21] op_sel_hi:[1,0]
	v_cvt_pk_bf16_f32 v1, v2, v3
	global_store_dwordx2 v[64:65], v[0:1], off offset:96
	global_load_dwordx4 v[0:3], v[186:187], off offset:224
	s_waitcnt vmcnt(0)
	v_pk_mul_f32 v[0:1], v[4:5], v[0:1]
	v_pk_mul_f32 v[4:5], v[14:15], v[20:21] op_sel_hi:[1,0]
	v_cvt_pk_bf16_f32 v0, v0, v1
	v_pk_mul_f32 v[2:3], v[4:5], v[2:3]
	s_branch .LBB0_617
